# C6 K-loop: after-load barrier only for waves 4-7, after-MFMA barrier only for waves 0-3 (half the barrier executions), offset barriers removed
# baseline (speedup 1.0000x reference)
.LBB0_2613:
	v_readlane_b32 s4, v253, 42
	v_readlane_b32 s5, v253, 43
	s_load_dwordx2 s[16:17], s[0:1], 0xa8
	s_waitcnt lgkmcnt(0)
	s_load_dwordx2 s[12:13], s[0:1], 0xa8
	s_waitcnt lgkmcnt(0)
	s_load_dwordx2 s[14:15], s[0:1], 0xa8
	s_waitcnt lgkmcnt(0)
	s_andn2_b64 vcc, exec, s[4:5]
	v_readfirstlane_b32 s4, v0
	s_cbranch_vccnz .LBB0_2633
	v_lshlrev_b32_e32 v2, 4, v0
	v_add_u32_e32 v3, 0x2000, v2
	v_ashrrev_i32_e32 v4, 31, v3
	v_lshrrev_b32_e32 v4, 22, v4
	v_add_u32_e32 v4, v3, v4
	v_ashrrev_i32_e32 v10, 10, v4
	v_mul_i32_i24_e32 v4, 0x400, v10
	v_sub_u32_e32 v3, v3, v4
	v_readlane_b32 s18, v255, 20
	v_lshrrev_b32_e32 v4, 4, v3
	v_readlane_b32 s19, v255, 21
	v_bitop3_b32 v3, v4, v3, 32 bitop3:0x6c
	s_and_b64 s[18:19], s[18:19], exec
	s_mov_b32 s5, 0x100000
	v_ashrrev_i32_e32 v4, 31, v3
	s_cselect_b32 s18, s5, 0x2c00000
	s_add_u32 s5, s6, s10
	v_lshrrev_b32_e32 v4, 26, v4
	s_addc_u32 s30, s7, s11
	v_add_u32_e32 v4, v3, v4
	v_lshlrev_b32_e32 v5, 3, v10
	s_add_u32 s6, s16, s18
	v_ashrrev_i32_e32 v11, 6, v4
	v_and_b32_e32 v5, -16, v5
	s_addc_u32 s7, s17, 0
	v_add_u32_e32 v5, v11, v5
	s_add_u32 s31, s6, 0xb80000
	v_and_b32_e32 v6, 3, v11
	s_mov_b32 s6, 0x1fffe0
	v_lshrrev_b32_e32 v7, 2, v5
	v_lshlrev_b32_e32 v8, 1, v5
	v_and_b32_e32 v4, 0xc0, v4
	v_and_or_b32 v6, v5, s6, v6
	v_and_b32_e32 v7, 4, v7
	v_and_b32_e32 v8, 24, v8
	v_sub_u32_e32 v3, v3, v4
	v_or3_b32 v6, v6, v7, v8
	v_lshlrev_b32_e32 v7, 5, v10
	v_ashrrev_i16_sdwa v3, v228, sext(v3) dst_sel:DWORD dst_unused:UNUSED_PAD src0_sel:DWORD src1_sel:BYTE_0
	v_and_b32_e32 v7, 32, v7
	v_bfe_i32 v12, v3, 0, 16
	v_add_lshl_u32 v3, v7, v12, 1
	v_lshl_add_u32 v158, v6, 11, v3
	v_lshl_add_u32 v160, v5, 11, v3
	v_bfe_i32 v3, v0, 27, 1
	v_lshrrev_b32_e32 v3, 22, v3
	v_add_u32_e32 v3, v2, v3
	v_and_b32_e32 v3, 0xfffffc00, v3
	v_sub_u32_e32 v2, v2, v3
	v_lshrrev_b32_e32 v3, 4, v2
	v_ashrrev_i32_e32 v4, 31, v0
	v_bitop3_b32 v2, v3, v2, 32 bitop3:0x6c
	v_lshrrev_b32_e32 v4, 26, v4
	v_ashrrev_i32_e32 v3, 31, v2
	v_add_u32_e32 v4, v0, v4
	v_lshrrev_b32_e32 v3, 26, v3
	s_waitcnt lgkmcnt(0)
	v_ashrrev_i32_e32 v14, 6, v4
	v_add_u32_e32 v3, v2, v3
	v_lshlrev_b32_e32 v4, 3, v14
	v_ashrrev_i32_e32 v13, 6, v3
	v_and_b32_e32 v4, -16, v4
	v_add_u32_e32 v4, v13, v4
	v_and_b32_e32 v5, 3, v13
	v_lshrrev_b32_e32 v6, 2, v4
	v_lshlrev_b32_e32 v7, 1, v4
	v_and_b32_e32 v3, 0xc0, v3
	s_addc_u32 s34, s7, 0
	s_ashr_i32 s17, s4, 6
	v_and_or_b32 v5, v4, s6, v5
	v_and_b32_e32 v6, 4, v6
	v_and_b32_e32 v7, 24, v7
	v_sub_u32_e32 v2, v2, v3
	s_ashr_i32 s16, s4, 8
	s_lshl_b32 s35, s17, 10
	v_or3_b32 v5, v5, v6, v7
	v_lshlrev_b32_e32 v6, 5, v14
	v_ashrrev_i16_sdwa v2, v228, sext(v2) dst_sel:DWORD dst_unused:UNUSED_PAD src0_sel:DWORD src1_sel:BYTE_0
	v_readlane_b32 s6, v253, 53
	v_and_b32_e32 v6, 32, v6
	v_bfe_i32 v15, v2, 0, 16
	v_readlane_b32 s7, v253, 54
	s_add_u32 s6, s31, s6
	v_add_lshl_u32 v2, v6, v15, 1
	s_addc_u32 s7, s34, s7
	s_add_i32 s36, s35, 0
	v_lshl_add_u32 v162, v5, 11, v2
	s_add_i32 m0, s36, 0x10000
	v_lshl_add_u32 v164, v4, 11, v2
	global_load_lds_dwordx4 v162, s[6:7]
	s_add_i32 m0, s36, 0x12000
	s_add_u32 s10, s6, 0x40000
	global_load_lds_dwordx4 v158, s[6:7]
	s_addc_u32 s11, s7, 0
	s_add_i32 m0, s36, 0x14000
	v_mov_b32_e32 v163, v1
	global_load_lds_dwordx4 v162, s[10:11]
	s_add_i32 m0, s36, 0x16000
	v_mov_b32_e32 v159, v1
	global_load_lds_dwordx4 v158, s[10:11]
	v_readlane_b32 s10, v254, 15
	v_readlane_b32 s11, v254, 16
	s_add_u32 s26, s5, s10
	s_addc_u32 s27, s30, s11
	s_add_i32 s37, s36, 0x2000
	s_mov_b32 m0, s36
	s_add_u32 s10, s26, 0x40000
	global_load_lds_dwordx4 v164, s[26:27]
	s_mov_b32 m0, s37
	s_addc_u32 s11, s27, 0
	s_add_i32 s42, s36, 0x4000
	global_load_lds_dwordx4 v160, s[26:27]
	s_mov_b32 m0, s42
	s_add_i32 s43, s36, 0x6000
	global_load_lds_dwordx4 v164, s[10:11]
	s_mov_b32 m0, s43
	v_mov_b32_e32 v165, v1
	global_load_lds_dwordx4 v160, s[10:11]
	v_mov_b32_e32 v161, v1
	s_cmp_eq_u32 s16, 1
	v_lshl_add_u64 v[8:9], s[6:7], 0, v[162:163]
	v_lshl_add_u64 v[6:7], s[6:7], 0, v[158:159]
	v_lshl_add_u64 v[2:3], s[26:27], 0, v[164:165]
	s_cselect_b64 s[10:11], -1, 0
	s_cmp_lg_u32 s16, 1
	v_lshl_add_u64 v[4:5], s[26:27], 0, v[160:161]
	s_cbranch_scc1 .LBB0_2616
.LBB0_2616:
	s_add_u32 s12, s12, 0xac00000
	s_addc_u32 s13, s13, 0
	s_add_u32 s14, s14, 0x1f00000
	s_addc_u32 s15, s15, 0
	s_lshl_b32 s17, s17, 5
	s_and_b32 s21, s17, 0x60
	s_add_i32 m0, s36, 0x18000
	v_lshl_add_u64 v[8:9], v[8:9], 0, s[56:57]
	s_lshl_b32 s20, s16, 13
	s_lshl_b32 s17, s21, 7
	s_waitcnt vmcnt(2)
	s_barrier
	global_load_lds_dwordx4 v[8:9], off
	v_lshl_add_u64 v[6:7], v[6:7], 0, s[56:57]
	s_add_i32 m0, s36, 0x1a000
	s_add_i32 s44, s36, 0x8000
	s_add_i32 s45, s36, 0xa000
	global_load_lds_dwordx4 v[6:7], off
	v_lshl_add_u64 v[2:3], v[2:3], 0, s[56:57]
	s_mov_b32 m0, s44
	s_add_u32 s18, s6, 0x40080
	global_load_lds_dwordx4 v[2:3], off
	v_lshl_add_u64 v[2:3], v[4:5], 0, s[56:57]
	s_mov_b32 m0, s45
	s_addc_u32 s19, s7, 0
	global_load_lds_dwordx4 v[2:3], off
	s_add_i32 m0, s36, 0x1c000
	v_lshl_add_u64 v[2:3], s[18:19], 0, v[162:163]
	global_load_lds_dwordx4 v[2:3], off
	v_lshl_add_u64 v[2:3], s[18:19], 0, v[158:159]
	s_add_i32 m0, s36, 0x1e000
	s_cmpk_lt_u32 s4, 0x100
	global_load_lds_dwordx4 v[2:3], off
	v_lshrrev_b32_e32 v3, 1, v0
	v_and_b32_e32 v3, 24, v3
	v_and_b32_e32 v2, 15, v0
	v_lshlrev_b32_e32 v4, 1, v3
	v_lshlrev_b32_e32 v0, 2, v0
	v_lshl_or_b32 v180, s16, 6, v2
	v_lshl_or_b32 v2, v2, 6, v4
	v_and_b32_e32 v0, 32, v0
	v_bitop3_b32 v4, v2, s20, v0 bitop3:0xde
	v_bitop3_b32 v181, v2, s17, v0 bitop3:0xde
	v_lshlrev_b32_e32 v0, 14, v10
	v_and_b32_e32 v0, 0xffff8000, v0
	v_lshl_add_u32 v0, v11, 11, v0
	v_and_b32_e32 v2, 1, v10
	v_lshl_or_b32 v0, v2, 6, v0
	v_lshl_add_u32 v166, v12, 1, v0
	v_lshlrev_b32_e32 v0, 14, v14
	v_and_b32_e32 v0, 0xffff8000, v0
	s_waitcnt vmcnt(6)
	v_lshl_add_u32 v0, v13, 11, v0
	v_and_b32_e32 v2, 1, v14
	v_lshl_or_b32 v0, v2, 6, v0
	v_readlane_b32 s18, v254, 13
	s_cselect_b64 s[16:17], -1, 0
	v_or_b32_e32 v182, s21, v3
	v_mov_b32_e32 v167, v1
	v_lshl_add_u32 v168, v15, 1, v0
	v_mov_b32_e32 v169, v1
	s_mov_b32 s46, 0
	v_add_u32_e32 v183, 0, v4
	v_readlane_b32 s47, v253, 52
	s_mov_b32 s4, s18
	s_barrier
	v_readlane_b32 s19, v254, 14
	s_branch .LBB0_2619

.LBB0_2626:
	s_add_u32 s26, s6, 0xfffc0080
	s_addc_u32 s27, s7, -1
	s_add_i32 s50, 0, 0x10000
	s_cmp_eq_u32 s49, 12
	s_cselect_b32 s29, s21, s27
	s_cselect_b32 s28, s33, s26
	v_add_u32_e32 v0, s50, v181
	s_cselect_b32 s27, s19, s48
	s_cselect_b32 s26, s40, s41
	s_add_i32 s58, 0, 0x14000
	ds_read_b128 v[130:133], v0
	ds_read_b128 v[134:137], v0 offset:1024
	ds_read_b128 v[138:141], v0 offset:2048
	ds_read_b128 v[142:145], v0 offset:3072
	v_add_u32_e32 v0, s58, v181
	ds_read_b128 v[146:149], v0
	ds_read_b128 v[150:153], v0 offset:1024
	ds_read_b128 v[154:157], v0 offset:2048
	ds_read_b128 v[170:173], v0 offset:3072
	v_lshl_add_u64 v[178:179], s[6:7], 0, v[168:169]
	s_add_i32 m0, s36, 0xc000
	ds_read_b128 v[174:177], v183
	ds_read_b128 v[184:187], v183 offset:1024
	ds_read_b128 v[188:191], v183 offset:2048
	ds_read_b128 v[192:195], v183 offset:3072
	ds_read_b128 v[196:199], v183 offset:4096
	ds_read_b128 v[200:203], v183 offset:5120
	ds_read_b128 v[204:207], v183 offset:6144
	ds_read_b128 v[216:219], v183 offset:7168
	global_load_lds_dwordx4 v[178:179], off
	v_lshl_add_u64 v[178:179], s[6:7], 0, v[166:167]
	s_add_i32 m0, s36, 0xe000
	s_nop 0
	global_load_lds_dwordx4 v[178:179], off
	s_waitcnt vmcnt(8)
	s_waitcnt lgkmcnt(0)
	s_and_b64 vcc, exec, s[10:11]
	s_cbranch_vccz .Lbskip_c6_1
	s_barrier
.Lbskip_c6_1:
	s_setprio 1
	s_waitcnt lgkmcnt(0)
	v_mfma_f32_16x16x32_bf16 v[126:129], v[130:133], v[174:177], v[126:129]
	v_mfma_f32_16x16x32_bf16 v[122:125], v[138:141], v[174:177], v[122:125]
	v_mfma_f32_16x16x32_bf16 v[110:113], v[130:133], v[188:191], v[110:113]
	v_mfma_f32_16x16x32_bf16 v[106:109], v[138:141], v[188:191], v[106:109]
	v_mfma_f32_16x16x32_bf16 v[94:97], v[130:133], v[196:199], v[94:97]
	v_mfma_f32_16x16x32_bf16 v[90:93], v[138:141], v[196:199], v[90:93]
	v_mfma_f32_16x16x32_bf16 v[78:81], v[130:133], v[204:207], v[78:81]
	v_mfma_f32_16x16x32_bf16 v[74:77], v[138:141], v[204:207], v[74:77]
	v_mfma_f32_16x16x32_bf16 v[126:129], v[134:137], v[184:187], v[126:129]
	v_mfma_f32_16x16x32_bf16 v[122:125], v[142:145], v[184:187], v[122:125]
	v_mfma_f32_16x16x32_bf16 v[110:113], v[134:137], v[192:195], v[110:113]
	v_mfma_f32_16x16x32_bf16 v[106:109], v[142:145], v[192:195], v[106:109]
	v_mfma_f32_16x16x32_bf16 v[94:97], v[134:137], v[200:203], v[94:97]
	v_mfma_f32_16x16x32_bf16 v[90:93], v[142:145], v[200:203], v[90:93]
	v_mfma_f32_16x16x32_bf16 v[78:81], v[134:137], v[216:219], v[78:81]
	v_mfma_f32_16x16x32_bf16 v[74:77], v[142:145], v[216:219], v[74:77]
	s_setprio 0
	s_setprio 1
	v_mfma_f32_16x16x32_bf16 v[118:121], v[146:149], v[174:177], v[118:121]
	v_mfma_f32_16x16x32_bf16 v[114:117], v[154:157], v[174:177], v[114:117]
	v_mfma_f32_16x16x32_bf16 v[102:105], v[146:149], v[188:191], v[102:105]
	v_mfma_f32_16x16x32_bf16 v[98:101], v[154:157], v[188:191], v[98:101]
	v_mfma_f32_16x16x32_bf16 v[86:89], v[146:149], v[196:199], v[86:89]
	v_mfma_f32_16x16x32_bf16 v[82:85], v[154:157], v[196:199], v[82:85]
	v_mfma_f32_16x16x32_bf16 v[70:73], v[146:149], v[204:207], v[70:73]
	v_mfma_f32_16x16x32_bf16 v[66:69], v[154:157], v[204:207], v[66:69]
	v_mfma_f32_16x16x32_bf16 v[118:121], v[150:153], v[184:187], v[118:121]
	v_mfma_f32_16x16x32_bf16 v[114:117], v[170:173], v[184:187], v[114:117]
	v_mfma_f32_16x16x32_bf16 v[102:105], v[150:153], v[192:195], v[102:105]
	v_mfma_f32_16x16x32_bf16 v[98:101], v[170:173], v[192:195], v[98:101]
	v_mfma_f32_16x16x32_bf16 v[86:89], v[150:153], v[200:203], v[86:89]
	v_mfma_f32_16x16x32_bf16 v[82:85], v[170:173], v[200:203], v[82:85]
	v_mfma_f32_16x16x32_bf16 v[70:73], v[150:153], v[216:219], v[70:73]
	v_mfma_f32_16x16x32_bf16 v[66:69], v[170:173], v[216:219], v[66:69]
	s_setprio 0
	s_and_b64 vcc, exec, s[16:17]
	s_cbranch_vccz .Lbskip_c6_2
	s_barrier
.Lbskip_c6_2:
	s_add_i32 s50, s50, s35
	v_lshl_add_u64 v[178:179], s[26:27], 0, v[162:163]
	s_mov_b32 m0, s50
	ds_read_b128 v[174:177], v183 offset:16384
	ds_read_b128 v[184:187], v183 offset:17408
	ds_read_b128 v[188:191], v183 offset:18432
	ds_read_b128 v[192:195], v183 offset:19456
	ds_read_b128 v[196:199], v183 offset:20480
	ds_read_b128 v[200:203], v183 offset:21504
	ds_read_b128 v[204:207], v183 offset:22528
	ds_read_b128 v[216:219], v183 offset:23552
	global_load_lds_dwordx4 v[178:179], off
	s_add_i32 m0, s50, 0x2000
	s_add_u32 s52, s26, 0x40000
	v_lshl_add_u64 v[208:209], s[26:27], 0, v[158:159]
	s_addc_u32 s53, s27, 0
	s_add_i32 s50, s58, s35
	global_load_lds_dwordx4 v[208:209], off
	v_lshl_add_u64 v[220:221], s[52:53], 0, v[162:163]
	s_mov_b32 m0, s50
	v_lshl_add_u64 v[222:223], s[28:29], 0, v[160:161]
	global_load_lds_dwordx4 v[220:221], off
	v_lshl_add_u64 v[220:221], s[52:53], 0, v[158:159]
	s_add_i32 m0, s50, 0x2000
	s_nop 0
	global_load_lds_dwordx4 v[220:221], off
	v_lshl_add_u64 v[220:221], s[28:29], 0, v[164:165]
	s_mov_b32 m0, s36
	s_nop 0
	global_load_lds_dwordx4 v[220:221], off
	s_mov_b32 m0, s37
	s_nop 0
	global_load_lds_dwordx4 v[222:223], off
	s_waitcnt vmcnt(8)
	s_waitcnt lgkmcnt(0)
	s_and_b64 vcc, exec, s[10:11]
	s_cbranch_vccz .Lbskip_c6_3
	s_barrier
.Lbskip_c6_3:
	s_setprio 1
	s_waitcnt lgkmcnt(0)
	v_mfma_f32_16x16x32_bf16 v[62:65], v[130:133], v[174:177], v[62:65]
	v_mfma_f32_16x16x32_bf16 v[58:61], v[138:141], v[174:177], v[58:61]
	v_mfma_f32_16x16x32_bf16 v[46:49], v[130:133], v[188:191], v[46:49]
	v_mfma_f32_16x16x32_bf16 v[42:45], v[138:141], v[188:191], v[42:45]
	v_mfma_f32_16x16x32_bf16 v[30:33], v[130:133], v[196:199], v[30:33]
	v_mfma_f32_16x16x32_bf16 v[26:29], v[138:141], v[196:199], v[26:29]
	v_mfma_f32_16x16x32_bf16 v[14:17], v[130:133], v[204:207], v[14:17]
	v_mfma_f32_16x16x32_bf16 v[10:13], v[138:141], v[204:207], v[10:13]
	v_mfma_f32_16x16x32_bf16 v[62:65], v[134:137], v[184:187], v[62:65]
	v_mfma_f32_16x16x32_bf16 v[58:61], v[142:145], v[184:187], v[58:61]
	v_mfma_f32_16x16x32_bf16 v[46:49], v[134:137], v[192:195], v[46:49]
	v_mfma_f32_16x16x32_bf16 v[42:45], v[142:145], v[192:195], v[42:45]
	v_mfma_f32_16x16x32_bf16 v[30:33], v[134:137], v[200:203], v[30:33]
	v_mfma_f32_16x16x32_bf16 v[26:29], v[142:145], v[200:203], v[26:29]
	v_mfma_f32_16x16x32_bf16 v[14:17], v[134:137], v[216:219], v[14:17]
	v_mfma_f32_16x16x32_bf16 v[10:13], v[142:145], v[216:219], v[10:13]
	s_setprio 0
	s_setprio 1
	v_mfma_f32_16x16x32_bf16 v[54:57], v[146:149], v[174:177], v[54:57]
	v_mfma_f32_16x16x32_bf16 v[50:53], v[154:157], v[174:177], v[50:53]
	v_mfma_f32_16x16x32_bf16 v[38:41], v[146:149], v[188:191], v[38:41]
	v_mfma_f32_16x16x32_bf16 v[34:37], v[154:157], v[188:191], v[34:37]
	v_mfma_f32_16x16x32_bf16 v[22:25], v[146:149], v[196:199], v[22:25]
	v_mfma_f32_16x16x32_bf16 v[18:21], v[154:157], v[196:199], v[18:21]
	v_mfma_f32_16x16x32_bf16 v[6:9], v[146:149], v[204:207], v[6:9]
	v_mfma_f32_16x16x32_bf16 v[2:5], v[154:157], v[204:207], v[2:5]
	v_mfma_f32_16x16x32_bf16 v[54:57], v[150:153], v[184:187], v[54:57]
	v_mfma_f32_16x16x32_bf16 v[50:53], v[170:173], v[184:187], v[50:53]
	v_mfma_f32_16x16x32_bf16 v[38:41], v[150:153], v[192:195], v[38:41]
	v_mfma_f32_16x16x32_bf16 v[34:37], v[170:173], v[192:195], v[34:37]
	v_mfma_f32_16x16x32_bf16 v[22:25], v[150:153], v[200:203], v[22:25]
	v_mfma_f32_16x16x32_bf16 v[18:21], v[170:173], v[200:203], v[18:21]
	v_mfma_f32_16x16x32_bf16 v[6:9], v[150:153], v[216:219], v[6:9]
	v_mfma_f32_16x16x32_bf16 v[2:5], v[170:173], v[216:219], v[2:5]
	s_setprio 0
	s_and_b64 vcc, exec, s[16:17]
	s_cbranch_vccz .Lbskip_c6_4
	s_barrier
.Lbskip_c6_4:
	s_add_i32 s50, 0, 0x18000
	v_add_u32_e32 v0, s50, v181
	s_add_i32 s52, 0, 0x1c000
	ds_read_b128 v[130:133], v0
	ds_read_b128 v[134:137], v0 offset:1024
	ds_read_b128 v[138:141], v0 offset:2048
	ds_read_b128 v[142:145], v0 offset:3072
	v_add_u32_e32 v0, s52, v181
	ds_read_b128 v[146:149], v0
	ds_read_b128 v[150:153], v0 offset:1024
	ds_read_b128 v[154:157], v0 offset:2048
	ds_read_b128 v[170:173], v0 offset:3072
	s_add_u32 s28, s28, 0x40000
	s_addc_u32 s29, s29, 0
	s_mov_b32 m0, s42
	v_lshl_add_u64 v[224:225], s[28:29], 0, v[164:165]
	ds_read_b128 v[174:177], v183 offset:32768
	ds_read_b128 v[184:187], v183 offset:33792
	ds_read_b128 v[188:191], v183 offset:34816
	ds_read_b128 v[192:195], v183 offset:35840
	ds_read_b128 v[196:199], v183 offset:36864
	ds_read_b128 v[200:203], v183 offset:37888
	ds_read_b128 v[204:207], v183 offset:38912
	ds_read_b128 v[216:219], v183 offset:39936
	global_load_lds_dwordx4 v[224:225], off
	v_lshl_add_u64 v[224:225], s[28:29], 0, v[160:161]
	s_mov_b32 m0, s43
	s_nop 0
	global_load_lds_dwordx4 v[224:225], off
	s_waitcnt vmcnt(8)
	s_waitcnt lgkmcnt(0)
	s_and_b64 vcc, exec, s[10:11]
	s_cbranch_vccz .Lbskip_c6_5
	s_barrier

.Lbskip_c6_6:
	s_add_i32 s28, s50, s35
	v_lshl_add_u64 v[178:179], v[178:179], 0, s[56:57]
	s_mov_b32 m0, s28
	ds_read_b128 v[174:177], v183 offset:49152
	ds_read_b128 v[184:187], v183 offset:50176
	ds_read_b128 v[188:191], v183 offset:51200
	ds_read_b128 v[192:195], v183 offset:52224
	ds_read_b128 v[196:199], v183 offset:53248
	ds_read_b128 v[200:203], v183 offset:54272
	ds_read_b128 v[204:207], v183 offset:55296
	ds_read_b128 v[216:219], v183 offset:56320
	global_load_lds_dwordx4 v[178:179], off
	s_add_i32 m0, s28, 0x2000
	s_add_u32 s26, s26, 0x40080
	v_lshl_add_u64 v[178:179], v[208:209], 0, s[56:57]
	s_addc_u32 s27, s27, 0
	s_add_i32 s28, s52, s35
	global_load_lds_dwordx4 v[178:179], off
	v_lshl_add_u64 v[178:179], s[26:27], 0, v[162:163]
	s_mov_b32 m0, s28
	s_nop 0
	global_load_lds_dwordx4 v[178:179], off
	v_lshl_add_u64 v[178:179], s[26:27], 0, v[158:159]
	s_add_i32 m0, s28, 0x2000
	s_nop 0
	global_load_lds_dwordx4 v[178:179], off
	v_lshl_add_u64 v[178:179], v[220:221], 0, s[56:57]
	s_mov_b32 m0, s44
	s_nop 0
	global_load_lds_dwordx4 v[178:179], off
	v_lshl_add_u64 v[178:179], v[222:223], 0, s[56:57]
	s_mov_b32 m0, s45
	s_nop 0
	global_load_lds_dwordx4 v[178:179], off
	s_waitcnt vmcnt(8)
	s_waitcnt lgkmcnt(0)
	s_and_b64 vcc, exec, s[10:11]
	s_cbranch_vccz .Lbskip_c6_7
	s_barrier

.Lbskip_c6_8:
	s_add_i32 s49, s49, 2
	s_add_u32 s41, s41, 0x100
	s_addc_u32 s48, s48, 0
	s_add_u32 s6, s6, 0x100
	s_addc_u32 s7, s7, 0
	s_cmp_gt_u32 s49, 13
	s_cbranch_scc0 .LBB0_2626
	s_and_b64 vcc, exec, s[16:17]
	s_cbranch_vccz .LBB0_2629
.LBB0_2629:
	v_mov_b32_e32 v204, 0
	v_mov_b32_e32 v205, 0
	v_mov_b32_e32 v206, 0
	v_mov_b32_e32 v207, 0
	v_lshl_add_u32 v178, s4, 8, v180
	v_and_b32_e32 v130, 8, v182
	v_and_b32_e32 v131, 16, v182
	v_lshlrev_b32_e32 v130, 2, v130
	v_lshl_add_u32 v130, v131, 3, v130
	v_add_u32_e32 v130, v130, v178
	v_mov_b32_e32 v131, 0
	v_lshl_add_u64 v[130:131], v[130:131], 4, s[14:15]
	global_load_dword v140, v[130:131], off offset:268
	s_waitcnt vmcnt(9)
	v_add_f32_e32 v240, v240, v241
	v_add_f32_e32 v242, v242, v243
	v_add_f32_e32 v240, v240, v242
	v_fmamk_f32 v240, v240, 0x3a800000, v226
	v_rsq_f32_e32 v240, v240
	v_and_b32_e32 v190, 15, v180
	v_lshlrev_b32_e32 v190, 2, v190
	v_add_u32_e32 v191, 64, v190
	v_add_u32_e32 v192, 0x80, v190
	v_add_u32_e32 v193, 0xc0, v190
	ds_bpermute_b32 v144, v190, v240
	ds_bpermute_b32 v148, v191, v240
	ds_bpermute_b32 v152, v192, v240
	ds_bpermute_b32 v156, v193, v240
	v_lshl_or_b32 v170, s47, 8, v182
	v_lshlrev_b32_e32 v170, 1, v170
	v_mov_b32_e32 v171, 0
	v_mov_b32_e32 v179, 0
	v_lshlrev_b64 v[172:173], 13, v[178:179]
	v_lshl_add_u64 v[172:173], s[12:13], 0, v[172:173]
	v_lshl_add_u64 v[172:173], v[172:173], 0, v[170:171]
	s_waitcnt lgkmcnt(0)
	v_pk_mul_f32 v[126:127], v[126:127], v[144:145] op_sel_hi:[1,0]
	v_pk_mul_f32 v[128:129], v[128:129], v[144:145] op_sel_hi:[1,0]
	v_pk_mul_f32 v[122:123], v[122:123], v[144:145] op_sel_hi:[1,0]
	v_pk_mul_f32 v[124:125], v[124:125], v[144:145] op_sel_hi:[1,0]
	v_max_f32_e32 v132, 0, v126
	v_max_f32_e32 v133, 0, v127
	v_max_f32_e32 v134, 0, v128
	v_max_f32_e32 v135, 0, v129
	v_max_f32_e32 v136, 0, v122
	v_max_f32_e32 v137, 0, v123
	v_max_f32_e32 v138, 0, v124
	v_max_f32_e32 v139, 0, v125
	v_pk_mul_f32 v[126:127], v[126:127], v[132:133]
	v_pk_mul_f32 v[128:129], v[128:129], v[134:135]
	v_pk_mul_f32 v[122:123], v[122:123], v[136:137]
	v_pk_mul_f32 v[124:125], v[124:125], v[138:139]
	v_cvt_pk_bf16_f32 v126, v126, v127
	v_cvt_pk_bf16_f32 v127, v128, v129
	v_cvt_pk_bf16_f32 v128, v122, v123
	v_cvt_pk_bf16_f32 v129, v124, v125
	global_store_dwordx4 v[172:173], v[126:129], off
	v_pk_mul_f32 v[118:119], v[118:119], v[144:145] op_sel_hi:[1,0]
	v_pk_mul_f32 v[120:121], v[120:121], v[144:145] op_sel_hi:[1,0]
	v_pk_mul_f32 v[114:115], v[114:115], v[144:145] op_sel_hi:[1,0]
	v_pk_mul_f32 v[116:117], v[116:117], v[144:145] op_sel_hi:[1,0]
	v_max_f32_e32 v132, 0, v118
	v_max_f32_e32 v133, 0, v119
	v_max_f32_e32 v134, 0, v120
	v_max_f32_e32 v135, 0, v121
	v_max_f32_e32 v136, 0, v114
	v_max_f32_e32 v137, 0, v115
	v_max_f32_e32 v138, 0, v116
	v_max_f32_e32 v139, 0, v117
	v_pk_mul_f32 v[118:119], v[118:119], v[132:133]
	v_pk_mul_f32 v[120:121], v[120:121], v[134:135]
	v_pk_mul_f32 v[114:115], v[114:115], v[136:137]
	v_pk_mul_f32 v[116:117], v[116:117], v[138:139]
	v_cvt_pk_bf16_f32 v118, v118, v119
	v_cvt_pk_bf16_f32 v119, v120, v121
	v_cvt_pk_bf16_f32 v120, v114, v115
	v_cvt_pk_bf16_f32 v121, v116, v117
	global_store_dwordx4 v[172:173], v[118:121], off offset:256
	s_mov_b64 s[40:41], 0x40000
	v_lshl_add_u64 v[176:177], v[172:173], 0, s[40:41]
	v_pk_mul_f32 v[94:95], v[94:95], v[148:149] op_sel_hi:[1,0]
	v_pk_mul_f32 v[96:97], v[96:97], v[148:149] op_sel_hi:[1,0]
	v_pk_mul_f32 v[90:91], v[90:91], v[148:149] op_sel_hi:[1,0]
	v_pk_mul_f32 v[92:93], v[92:93], v[148:149] op_sel_hi:[1,0]
	v_max_f32_e32 v132, 0, v94
	v_max_f32_e32 v133, 0, v95
	v_max_f32_e32 v134, 0, v96
	v_max_f32_e32 v135, 0, v97
	v_max_f32_e32 v136, 0, v90
	v_max_f32_e32 v137, 0, v91
	v_max_f32_e32 v138, 0, v92
	v_max_f32_e32 v139, 0, v93
	v_pk_mul_f32 v[94:95], v[94:95], v[132:133]
	v_pk_mul_f32 v[96:97], v[96:97], v[134:135]
	v_pk_mul_f32 v[90:91], v[90:91], v[136:137]
	v_pk_mul_f32 v[92:93], v[92:93], v[138:139]
	v_cvt_pk_bf16_f32 v94, v94, v95
	v_cvt_pk_bf16_f32 v95, v96, v97
	v_cvt_pk_bf16_f32 v96, v90, v91
	v_cvt_pk_bf16_f32 v97, v92, v93
	global_store_dwordx4 v[176:177], v[94:97], off
	v_pk_mul_f32 v[86:87], v[86:87], v[148:149] op_sel_hi:[1,0]
	v_pk_mul_f32 v[88:89], v[88:89], v[148:149] op_sel_hi:[1,0]
	v_pk_mul_f32 v[82:83], v[82:83], v[148:149] op_sel_hi:[1,0]
	v_pk_mul_f32 v[84:85], v[84:85], v[148:149] op_sel_hi:[1,0]
	v_max_f32_e32 v132, 0, v86
	v_max_f32_e32 v133, 0, v87
	v_max_f32_e32 v134, 0, v88
	v_max_f32_e32 v135, 0, v89
	v_max_f32_e32 v136, 0, v82
	v_max_f32_e32 v137, 0, v83
	v_max_f32_e32 v138, 0, v84
	v_max_f32_e32 v139, 0, v85
	v_pk_mul_f32 v[86:87], v[86:87], v[132:133]
	v_pk_mul_f32 v[88:89], v[88:89], v[134:135]
	v_pk_mul_f32 v[82:83], v[82:83], v[136:137]
	v_pk_mul_f32 v[84:85], v[84:85], v[138:139]
	v_cvt_pk_bf16_f32 v86, v86, v87
	v_cvt_pk_bf16_f32 v87, v88, v89
	v_cvt_pk_bf16_f32 v88, v82, v83
	v_cvt_pk_bf16_f32 v89, v84, v85
	global_store_dwordx4 v[176:177], v[86:89], off offset:256
	s_mov_b64 s[40:41], 0x100000
	v_lshl_add_u64 v[174:175], v[172:173], 0, s[40:41]
	v_pk_mul_f32 v[62:63], v[62:63], v[152:153] op_sel_hi:[1,0]
	v_pk_mul_f32 v[64:65], v[64:65], v[152:153] op_sel_hi:[1,0]
	v_pk_mul_f32 v[58:59], v[58:59], v[152:153] op_sel_hi:[1,0]
	v_pk_mul_f32 v[60:61], v[60:61], v[152:153] op_sel_hi:[1,0]
	v_max_f32_e32 v132, 0, v62
	v_max_f32_e32 v133, 0, v63
	v_max_f32_e32 v134, 0, v64
	v_max_f32_e32 v135, 0, v65
	v_max_f32_e32 v136, 0, v58
	v_max_f32_e32 v137, 0, v59
	v_max_f32_e32 v138, 0, v60
	v_max_f32_e32 v139, 0, v61
	v_pk_mul_f32 v[62:63], v[62:63], v[132:133]
	v_pk_mul_f32 v[64:65], v[64:65], v[134:135]
	v_pk_mul_f32 v[58:59], v[58:59], v[136:137]
	v_pk_mul_f32 v[60:61], v[60:61], v[138:139]
	v_cvt_pk_bf16_f32 v62, v62, v63
	v_cvt_pk_bf16_f32 v63, v64, v65
	v_cvt_pk_bf16_f32 v64, v58, v59
	v_cvt_pk_bf16_f32 v65, v60, v61
	global_store_dwordx4 v[174:175], v[62:65], off
	v_pk_mul_f32 v[54:55], v[54:55], v[152:153] op_sel_hi:[1,0]
	v_pk_mul_f32 v[56:57], v[56:57], v[152:153] op_sel_hi:[1,0]
	v_pk_mul_f32 v[50:51], v[50:51], v[152:153] op_sel_hi:[1,0]
	v_pk_mul_f32 v[52:53], v[52:53], v[152:153] op_sel_hi:[1,0]
	v_max_f32_e32 v132, 0, v54
	v_max_f32_e32 v133, 0, v55
	v_max_f32_e32 v134, 0, v56
	v_max_f32_e32 v135, 0, v57
	v_max_f32_e32 v136, 0, v50
	v_max_f32_e32 v137, 0, v51
	v_max_f32_e32 v138, 0, v52
	v_max_f32_e32 v139, 0, v53
	v_pk_mul_f32 v[54:55], v[54:55], v[132:133]
	v_pk_mul_f32 v[56:57], v[56:57], v[134:135]
	v_pk_mul_f32 v[50:51], v[50:51], v[136:137]
	v_pk_mul_f32 v[52:53], v[52:53], v[138:139]
	v_cvt_pk_bf16_f32 v54, v54, v55
	v_cvt_pk_bf16_f32 v55, v56, v57
	v_cvt_pk_bf16_f32 v56, v50, v51
	v_cvt_pk_bf16_f32 v57, v52, v53
	global_store_dwordx4 v[174:175], v[54:57], off offset:256
	s_mov_b64 s[40:41], 0x140000
	v_lshl_add_u64 v[176:177], v[172:173], 0, s[40:41]
	v_pk_mul_f32 v[30:31], v[30:31], v[156:157] op_sel_hi:[1,0]
	v_pk_mul_f32 v[32:33], v[32:33], v[156:157] op_sel_hi:[1,0]
	v_pk_mul_f32 v[26:27], v[26:27], v[156:157] op_sel_hi:[1,0]
	v_pk_mul_f32 v[28:29], v[28:29], v[156:157] op_sel_hi:[1,0]
	v_max_f32_e32 v132, 0, v30
	v_max_f32_e32 v133, 0, v31
	v_max_f32_e32 v134, 0, v32
	v_max_f32_e32 v135, 0, v33
	v_max_f32_e32 v136, 0, v26
	v_max_f32_e32 v137, 0, v27
	v_max_f32_e32 v138, 0, v28
	v_max_f32_e32 v139, 0, v29
	v_pk_mul_f32 v[30:31], v[30:31], v[132:133]
	v_pk_mul_f32 v[32:33], v[32:33], v[134:135]
	v_pk_mul_f32 v[26:27], v[26:27], v[136:137]
	v_pk_mul_f32 v[28:29], v[28:29], v[138:139]
	v_cvt_pk_bf16_f32 v30, v30, v31
	v_cvt_pk_bf16_f32 v31, v32, v33
	v_cvt_pk_bf16_f32 v32, v26, v27
	v_cvt_pk_bf16_f32 v33, v28, v29
	global_store_dwordx4 v[176:177], v[30:33], off
	v_pk_mul_f32 v[22:23], v[22:23], v[156:157] op_sel_hi:[1,0]
	v_pk_mul_f32 v[24:25], v[24:25], v[156:157] op_sel_hi:[1,0]
	v_pk_mul_f32 v[18:19], v[18:19], v[156:157] op_sel_hi:[1,0]
	v_pk_mul_f32 v[20:21], v[20:21], v[156:157] op_sel_hi:[1,0]
	v_max_f32_e32 v132, 0, v22
	v_max_f32_e32 v133, 0, v23
	v_max_f32_e32 v134, 0, v24
	v_max_f32_e32 v135, 0, v25
	v_max_f32_e32 v136, 0, v18
	v_max_f32_e32 v137, 0, v19
	v_max_f32_e32 v138, 0, v20
	v_max_f32_e32 v139, 0, v21
	v_pk_mul_f32 v[22:23], v[22:23], v[132:133]
	v_pk_mul_f32 v[24:25], v[24:25], v[134:135]
	v_pk_mul_f32 v[18:19], v[18:19], v[136:137]
	v_pk_mul_f32 v[20:21], v[20:21], v[138:139]
	v_cvt_pk_bf16_f32 v22, v22, v23
	v_cvt_pk_bf16_f32 v23, v24, v25
	v_cvt_pk_bf16_f32 v24, v18, v19
	v_cvt_pk_bf16_f32 v25, v20, v21
	global_store_dwordx4 v[176:177], v[22:25], off offset:256
	s_waitcnt vmcnt(8)
	v_add_f32_e32 v244, v244, v245
	v_add_f32_e32 v239, v239, v140
	v_add_f32_e32 v244, v244, v239
	v_fmamk_f32 v244, v244, 0x3a800000, v226
	v_rsq_f32_e32 v244, v244
	s_nop 0
	ds_bpermute_b32 v146, v190, v244
	ds_bpermute_b32 v150, v191, v244
	ds_bpermute_b32 v154, v192, v244
	ds_bpermute_b32 v194, v193, v244
	s_waitcnt lgkmcnt(0)
	s_mov_b64 s[40:41], 0x20000
	v_lshl_add_u64 v[174:175], v[172:173], 0, s[40:41]
	v_pk_mul_f32 v[110:111], v[110:111], v[146:147] op_sel_hi:[1,0]
	v_pk_mul_f32 v[112:113], v[112:113], v[146:147] op_sel_hi:[1,0]
	v_pk_mul_f32 v[106:107], v[106:107], v[146:147] op_sel_hi:[1,0]
	v_pk_mul_f32 v[108:109], v[108:109], v[146:147] op_sel_hi:[1,0]
	v_max_f32_e32 v132, 0, v110
	v_max_f32_e32 v133, 0, v111
	v_max_f32_e32 v134, 0, v112
	v_max_f32_e32 v135, 0, v113
	v_max_f32_e32 v136, 0, v106
	v_max_f32_e32 v137, 0, v107
	v_max_f32_e32 v138, 0, v108
	v_max_f32_e32 v139, 0, v109
	v_pk_mul_f32 v[110:111], v[110:111], v[132:133]
	v_pk_mul_f32 v[112:113], v[112:113], v[134:135]
	v_pk_mul_f32 v[106:107], v[106:107], v[136:137]
	v_pk_mul_f32 v[108:109], v[108:109], v[138:139]
	v_cvt_pk_bf16_f32 v110, v110, v111
	v_cvt_pk_bf16_f32 v111, v112, v113
	v_cvt_pk_bf16_f32 v112, v106, v107
	v_cvt_pk_bf16_f32 v113, v108, v109
	global_store_dwordx4 v[174:175], v[110:113], off
	v_pk_mul_f32 v[102:103], v[102:103], v[146:147] op_sel_hi:[1,0]
	v_pk_mul_f32 v[104:105], v[104:105], v[146:147] op_sel_hi:[1,0]
	v_pk_mul_f32 v[98:99], v[98:99], v[146:147] op_sel_hi:[1,0]
	v_pk_mul_f32 v[100:101], v[100:101], v[146:147] op_sel_hi:[1,0]
	v_max_f32_e32 v132, 0, v102
	v_max_f32_e32 v133, 0, v103
	v_max_f32_e32 v134, 0, v104
	v_max_f32_e32 v135, 0, v105
	v_max_f32_e32 v136, 0, v98
	v_max_f32_e32 v137, 0, v99
	v_max_f32_e32 v138, 0, v100
	v_max_f32_e32 v139, 0, v101
	v_pk_mul_f32 v[102:103], v[102:103], v[132:133]
	v_pk_mul_f32 v[104:105], v[104:105], v[134:135]
	v_pk_mul_f32 v[98:99], v[98:99], v[136:137]
	v_pk_mul_f32 v[100:101], v[100:101], v[138:139]
	v_cvt_pk_bf16_f32 v102, v102, v103
	v_cvt_pk_bf16_f32 v103, v104, v105
	v_cvt_pk_bf16_f32 v104, v98, v99
	v_cvt_pk_bf16_f32 v105, v100, v101
	global_store_dwordx4 v[174:175], v[102:105], off offset:256
	s_mov_b64 s[40:41], 0x60000
	v_lshl_add_u64 v[176:177], v[172:173], 0, s[40:41]
	v_pk_mul_f32 v[78:79], v[78:79], v[150:151] op_sel_hi:[1,0]
	v_pk_mul_f32 v[80:81], v[80:81], v[150:151] op_sel_hi:[1,0]
	v_pk_mul_f32 v[74:75], v[74:75], v[150:151] op_sel_hi:[1,0]
	v_pk_mul_f32 v[76:77], v[76:77], v[150:151] op_sel_hi:[1,0]
	v_max_f32_e32 v132, 0, v78
	v_max_f32_e32 v133, 0, v79
	v_max_f32_e32 v134, 0, v80
	v_max_f32_e32 v135, 0, v81
	v_max_f32_e32 v136, 0, v74
	v_max_f32_e32 v137, 0, v75
	v_max_f32_e32 v138, 0, v76
	v_max_f32_e32 v139, 0, v77
	v_pk_mul_f32 v[78:79], v[78:79], v[132:133]
	v_pk_mul_f32 v[80:81], v[80:81], v[134:135]
	v_pk_mul_f32 v[74:75], v[74:75], v[136:137]
	v_pk_mul_f32 v[76:77], v[76:77], v[138:139]
	v_cvt_pk_bf16_f32 v78, v78, v79
	v_cvt_pk_bf16_f32 v79, v80, v81
	v_cvt_pk_bf16_f32 v80, v74, v75
	v_cvt_pk_bf16_f32 v81, v76, v77
	global_store_dwordx4 v[176:177], v[78:81], off
	v_pk_mul_f32 v[70:71], v[70:71], v[150:151] op_sel_hi:[1,0]
	v_pk_mul_f32 v[72:73], v[72:73], v[150:151] op_sel_hi:[1,0]
	v_pk_mul_f32 v[66:67], v[66:67], v[150:151] op_sel_hi:[1,0]
	v_pk_mul_f32 v[68:69], v[68:69], v[150:151] op_sel_hi:[1,0]
	v_max_f32_e32 v132, 0, v70
	v_max_f32_e32 v133, 0, v71
	v_max_f32_e32 v134, 0, v72
	v_max_f32_e32 v135, 0, v73
	v_max_f32_e32 v136, 0, v66
	v_max_f32_e32 v137, 0, v67
	v_max_f32_e32 v138, 0, v68
	v_max_f32_e32 v139, 0, v69
	v_pk_mul_f32 v[70:71], v[70:71], v[132:133]
	v_pk_mul_f32 v[72:73], v[72:73], v[134:135]
	v_pk_mul_f32 v[66:67], v[66:67], v[136:137]
	v_pk_mul_f32 v[68:69], v[68:69], v[138:139]
	v_cvt_pk_bf16_f32 v70, v70, v71
	v_cvt_pk_bf16_f32 v71, v72, v73
	v_cvt_pk_bf16_f32 v72, v66, v67
	v_cvt_pk_bf16_f32 v73, v68, v69
	global_store_dwordx4 v[176:177], v[70:73], off offset:256
	s_mov_b64 s[40:41], 0x120000
	v_lshl_add_u64 v[174:175], v[172:173], 0, s[40:41]
	v_pk_mul_f32 v[46:47], v[46:47], v[154:155] op_sel_hi:[1,0]
	v_pk_mul_f32 v[48:49], v[48:49], v[154:155] op_sel_hi:[1,0]
	v_pk_mul_f32 v[42:43], v[42:43], v[154:155] op_sel_hi:[1,0]
	v_pk_mul_f32 v[44:45], v[44:45], v[154:155] op_sel_hi:[1,0]
	v_max_f32_e32 v132, 0, v46
	v_max_f32_e32 v133, 0, v47
	v_max_f32_e32 v134, 0, v48
	v_max_f32_e32 v135, 0, v49
	v_max_f32_e32 v136, 0, v42
	v_max_f32_e32 v137, 0, v43
	v_max_f32_e32 v138, 0, v44
	v_max_f32_e32 v139, 0, v45
	v_pk_mul_f32 v[46:47], v[46:47], v[132:133]
	v_pk_mul_f32 v[48:49], v[48:49], v[134:135]
	v_pk_mul_f32 v[42:43], v[42:43], v[136:137]
	v_pk_mul_f32 v[44:45], v[44:45], v[138:139]
	v_cvt_pk_bf16_f32 v46, v46, v47
	v_cvt_pk_bf16_f32 v47, v48, v49
	v_cvt_pk_bf16_f32 v48, v42, v43
	v_cvt_pk_bf16_f32 v49, v44, v45
	global_store_dwordx4 v[174:175], v[46:49], off
	v_pk_mul_f32 v[38:39], v[38:39], v[154:155] op_sel_hi:[1,0]
	v_pk_mul_f32 v[40:41], v[40:41], v[154:155] op_sel_hi:[1,0]
	v_pk_mul_f32 v[34:35], v[34:35], v[154:155] op_sel_hi:[1,0]
	v_pk_mul_f32 v[36:37], v[36:37], v[154:155] op_sel_hi:[1,0]
	v_max_f32_e32 v132, 0, v38
	v_max_f32_e32 v133, 0, v39
	v_max_f32_e32 v134, 0, v40
	v_max_f32_e32 v135, 0, v41
	v_max_f32_e32 v136, 0, v34
	v_max_f32_e32 v137, 0, v35
	v_max_f32_e32 v138, 0, v36
	v_max_f32_e32 v139, 0, v37
	v_pk_mul_f32 v[38:39], v[38:39], v[132:133]
	v_pk_mul_f32 v[40:41], v[40:41], v[134:135]
	v_pk_mul_f32 v[34:35], v[34:35], v[136:137]
	v_pk_mul_f32 v[36:37], v[36:37], v[138:139]
	v_cvt_pk_bf16_f32 v38, v38, v39
	v_cvt_pk_bf16_f32 v39, v40, v41
	v_cvt_pk_bf16_f32 v40, v34, v35
	v_cvt_pk_bf16_f32 v41, v36, v37
	global_store_dwordx4 v[174:175], v[38:41], off offset:256
	s_mov_b64 s[40:41], 0x160000
	v_lshl_add_u64 v[176:177], v[172:173], 0, s[40:41]
	v_pk_mul_f32 v[14:15], v[14:15], v[194:195] op_sel_hi:[1,0]
	v_pk_mul_f32 v[16:17], v[16:17], v[194:195] op_sel_hi:[1,0]
	v_pk_mul_f32 v[10:11], v[10:11], v[194:195] op_sel_hi:[1,0]
	v_pk_mul_f32 v[12:13], v[12:13], v[194:195] op_sel_hi:[1,0]
	v_max_f32_e32 v132, 0, v14
	v_max_f32_e32 v133, 0, v15
	v_max_f32_e32 v134, 0, v16
	v_max_f32_e32 v135, 0, v17
	v_max_f32_e32 v136, 0, v10
	v_max_f32_e32 v137, 0, v11
	v_max_f32_e32 v138, 0, v12
	v_max_f32_e32 v139, 0, v13
	v_pk_mul_f32 v[14:15], v[14:15], v[132:133]
	v_pk_mul_f32 v[16:17], v[16:17], v[134:135]
	v_pk_mul_f32 v[10:11], v[10:11], v[136:137]
	v_pk_mul_f32 v[12:13], v[12:13], v[138:139]
	v_cvt_pk_bf16_f32 v14, v14, v15
	v_cvt_pk_bf16_f32 v15, v16, v17
	v_cvt_pk_bf16_f32 v16, v10, v11
	v_cvt_pk_bf16_f32 v17, v12, v13
	global_store_dwordx4 v[176:177], v[14:17], off
	v_pk_mul_f32 v[6:7], v[6:7], v[194:195] op_sel_hi:[1,0]
	v_pk_mul_f32 v[8:9], v[8:9], v[194:195] op_sel_hi:[1,0]
	v_pk_mul_f32 v[2:3], v[2:3], v[194:195] op_sel_hi:[1,0]
	v_pk_mul_f32 v[4:5], v[4:5], v[194:195] op_sel_hi:[1,0]
	v_max_f32_e32 v132, 0, v6
	v_max_f32_e32 v133, 0, v7
	v_max_f32_e32 v134, 0, v8
	v_max_f32_e32 v135, 0, v9
	v_max_f32_e32 v136, 0, v2
	v_max_f32_e32 v137, 0, v3
	v_max_f32_e32 v138, 0, v4
	v_max_f32_e32 v139, 0, v5
	v_pk_mul_f32 v[6:7], v[6:7], v[132:133]
	v_pk_mul_f32 v[8:9], v[8:9], v[134:135]
	v_pk_mul_f32 v[2:3], v[2:3], v[136:137]
	v_pk_mul_f32 v[4:5], v[4:5], v[138:139]
	v_cvt_pk_bf16_f32 v6, v6, v7
	v_cvt_pk_bf16_f32 v7, v8, v9
	v_cvt_pk_bf16_f32 v8, v2, v3
	v_cvt_pk_bf16_f32 v9, v4, v5
	global_store_dwordx4 v[176:177], v[6:9], off offset:256
	s_nop 3
	v_mfma_f32_32x32x16_bf16 v[2:17], v[204:207], v[204:207], 0
	v_mfma_f32_32x32x16_bf16 v[18:33], v[204:207], v[204:207], 0
	v_mfma_f32_32x32x16_bf16 v[34:49], v[204:207], v[204:207], 0
	v_mfma_f32_32x32x16_bf16 v[50:65], v[204:207], v[204:207], 0
	v_mfma_f32_32x32x16_bf16 v[66:81], v[204:207], v[204:207], 0
	v_mfma_f32_32x32x16_bf16 v[82:97], v[204:207], v[204:207], 0
	v_mfma_f32_32x32x16_bf16 v[98:113], v[204:207], v[204:207], 0
	v_mfma_f32_32x32x16_bf16 v[114:129], v[204:207], v[204:207], 0
	s_mov_b64 s[6:7], -1
	s_andn2_b64 vcc, exec, s[38:39]
	s_cbranch_vccnz .LBB0_2618
	s_andn2_b64 vcc, exec, s[10:11]
	s_cbranch_vccnz .LBB0_2617
	s_branch .LBB0_2617
